# speedup vs baseline: 1.0136x; 1.0136x over previous
_Z9fast_mainILb0EEvPKiS1_S1_PKfPKcS3_PfS6_PiPyS6_:
	s_nop 0
	s_load_dwordx4 s[4:7], s[0:1], 0x20
	s_load_dwordx4 s[8:11], s[0:1], 0x8
	s_load_dwordx2 s[16:17], s[0:1], 0x0
	v_and_b32_e32 v1, 63, v0
	v_lshrrev_b32_e32 v8, 6, v0
	v_lshlrev_b32_e32 v150, 4, v1
	v_lshl_or_b32 v14, s2, 3, v8
	v_lshlrev_b32_e32 v14, 10, v14
	v_or_b32_e32 v14, v14, v150
	v_add_u32_e32 v212, 0x10000, v150
	v_add_u32_e32 v213, 0x18c00, v150
	v_mov_b32_e32 v151, 0
	s_waitcnt lgkmcnt(0)
	global_load_dwordx4 v[20:23], v14, s[16:17]
	v_lshl_add_u64 v[4:5], s[4:5], 0, v[150:151]
	v_lshlrev_b32_e32 v2, 10, v8
	v_mov_b32_e32 v3, v151
	v_lshl_add_u64 v[6:7], v[4:5], 0, v[2:3]
	v_readfirstlane_b32 s3, v2
	v_or_b32_e32 v3, 0x2000, v2
	s_mov_b32 m0, s3
	s_mov_b64 s[4:5], 0x2000
	v_readfirstlane_b32 s3, v3
	global_load_lds_dwordx4 v[6:7], off
	v_lshl_add_u64 v[10:11], v[6:7], 0, s[4:5]
	s_mov_b32 m0, s3
	v_or_b32_e32 v3, 0x6000, v2
	global_load_lds_dwordx4 v[10:11], off
	v_or_b32_e32 v10, 0x4000, v2
	v_mov_b32_e32 v11, v151
	v_readfirstlane_b32 s3, v10
	v_lshl_add_u64 v[12:13], v[4:5], 0, v[10:11]
	s_mov_b32 m0, s3
	s_mov_b64 s[4:5], 0x6000
	v_readfirstlane_b32 s3, v3
	global_load_lds_dwordx4 v[12:13], off
	v_lshl_add_u64 v[10:11], v[6:7], 0, s[4:5]
	s_mov_b32 m0, s3
	v_or_b32_e32 v3, 0xa000, v2
	global_load_lds_dwordx4 v[10:11], off
	v_or_b32_e32 v10, 0x8000, v2
	v_mov_b32_e32 v11, v151
	v_readfirstlane_b32 s3, v10
	v_lshl_add_u64 v[12:13], v[4:5], 0, v[10:11]
	s_mov_b32 m0, s3
	s_mov_b64 s[4:5], 0xa000
	v_readfirstlane_b32 s3, v3
	global_load_lds_dwordx4 v[12:13], off
	v_lshl_add_u64 v[10:11], v[6:7], 0, s[4:5]
	s_mov_b32 m0, s3
	v_or_b32_e32 v3, 0xe000, v2
	global_load_lds_dwordx4 v[10:11], off
	v_or_b32_e32 v10, 0xc000, v2
	v_mov_b32_e32 v11, v151
	v_readfirstlane_b32 s3, v10
	v_lshl_add_u64 v[12:13], v[4:5], 0, v[10:11]
	s_mov_b32 m0, s3
	s_mov_b64 s[4:5], 0xe000
	v_readfirstlane_b32 s3, v3
	global_load_lds_dwordx4 v[12:13], off
	v_lshl_add_u64 v[10:11], v[6:7], 0, s[4:5]
	s_mov_b32 m0, s3
	v_or_b32_e32 v3, 0x12000, v2
	global_load_lds_dwordx4 v[10:11], off
	v_or_b32_e32 v10, 0x10000, v2
	v_mov_b32_e32 v11, v151
	v_readfirstlane_b32 s3, v10
	v_lshl_add_u64 v[12:13], v[4:5], 0, v[10:11]
	s_mov_b32 m0, s3
	s_mov_b64 s[4:5], 0x12000
	v_readfirstlane_b32 s3, v3
	global_load_lds_dwordx4 v[12:13], off
	v_lshl_add_u64 v[10:11], v[6:7], 0, s[4:5]
	s_mov_b32 m0, s3
	s_nop 0
	global_load_lds_dwordx4 v[10:11], off
	v_or_b32_e32 v10, 0x14000, v2
	v_mov_b32_e32 v11, v151
	v_readfirstlane_b32 s3, v10
	v_lshl_add_u64 v[12:13], v[4:5], 0, v[10:11]
	s_mov_b32 m0, s3
	s_movk_i32 s3, 0x2c0
	global_load_lds_dwordx4 v[12:13], off
	v_cmp_gt_u32_e32 vcc, s3, v0
	s_and_saveexec_b64 s[4:5], vcc
	s_cbranch_execz .LBB1_2
	v_or_b32_e32 v3, 0x16000, v2
	s_mov_b64 s[12:13], 0x16000
	v_readfirstlane_b32 s3, v3
	v_lshl_add_u64 v[6:7], v[6:7], 0, s[12:13]
	s_mov_b32 m0, s3
	s_nop 0
	global_load_lds_dwordx4 v[6:7], off
